# out_proj epilogue: second batch of x rows prefetched with the first (one HBM round trip less per unit)
# speedup vs baseline: 1.0019x; 1.0019x over previous
; __device__ __forceinline__ unsigned cvt_pk_bf16(float lo, float hi) { const f32x2_t v = {lo, hi}; return __builtin_bit_cast(unsigned, __builtin_convertvector(v, bf16x2_t)); }
;     __device__ __forceinline__ void operator()(const f32x4 (&acc)[2][2][4][2], const Unit& u, int wr, int wc, int fr, int fq) const {
;         const int row0 = u.t * 256 + wr * 64 + fr, col0 = u.nt * 256 + wc * 32 + 8 * fq;
;         const int b = (u.t * 256) / SEQ;
;         f32x4 g[2][2];
; #pragma unroll
;         for (int bj = 0; bj < 2; ++bj)
; #pragma unroll
;             for (int n = 0; n < 2; ++n) g[bj][n] = *(const f32x4*)(gate + (size_t)b * 6144 + col0 + bj * 128 + 4 * n);
;         bf16_t* hb = h_row(out, ws, u.t * 256) + (size_t)(wr * 64 + fr) * D + col0;
; #pragma unroll
;         for (int ai = 0; ai < 2; ++ai)
; #pragma unroll
;             for (int mh = 0; mh < 2; ++mh) {
;                 f32x4 xv[2][2][2];
; #pragma unroll
;                 for (int m2 = 0; m2 < 2; ++m2) { const size_t off = (size_t)(row0 + ai * 128 + (2 * mh + m2) * 16) * D + col0;
; #pragma unroll
;                     for (int bj = 0; bj < 2; ++bj) { xv[m2][bj][0] = __builtin_nontemporal_load((const f32x4*)(x + off + bj * 128)); xv[m2][bj][1] = __builtin_nontemporal_load((const f32x4*)(x + off + bj * 128 + 4)); } }
; #pragma unroll
;                 for (int m2 = 0; m2 < 2; ++m2) { const int m = 2 * mh + m2;
; #pragma unroll
;                     for (int bj = 0; bj < 2; ++bj) {
;                         const f32x4 h0 = xv[m2][bj][0] + g[bj][0] * acc[ai][bj][m][0], h1 = xv[m2][bj][1] + g[bj][1] * acc[ai][bj][m][1];
;                         u32x4 w; w.x = cvt_pk_bf16(h0[0], h0[1]); w.y = cvt_pk_bf16(h0[2], h0[3]); w.z = cvt_pk_bf16(h1[0], h1[1]); w.w = cvt_pk_bf16(h1[2], h1[3]);
;                         *(u32x4*)(hb + (size_t)(ai * 128 + m * 16) * D + bj * 128) = w; } } }
.LBB0_436:
	s_ashr_i32 s27, s34, 31
	s_lshr_b32 s27, s27, 28
	s_add_i32 s27, s34, s27
	s_lshl_b32 s25, s34, 8
	s_ashr_i32 s27, s27, 4
	v_lshl_or_b32 v20, s78, 8, v171
	s_mul_hi_i32 s37, s27, 0x6000
	s_mulk_i32 s27, 0x6000
	v_add_u32_e32 v208, s25, v170
	s_add_u32 s36, s52, s27
	v_ashrrev_i32_e32 v21, 31, v20
	v_or_b32_e32 v186, 16, v208
	s_addc_u32 s37, s53, s37
	v_lshlrev_b64 v[10:11], 2, v[20:21]
	v_ashrrev_i32_e32 v209, 31, v208
	v_ashrrev_i32_e32 v187, 31, v186
	v_lshl_add_u64 v[14:15], s[36:37], 0, v[10:11]
	v_lshl_add_u64 v[210:211], s[10:11], 0, v[10:11]
	v_lshlrev_b64 v[10:11], 12, v[208:209]
	v_lshlrev_b64 v[186:187], 12, v[186:187]
	s_nop 15
	s_nop 15
	v_lshl_add_u64 v[18:19], v[210:211], 0, v[10:11]
	v_lshl_add_u64 v[204:205], v[210:211], 0, v[186:187]
	global_load_dwordx4 v[2:5], v[14:15], off offset:16
	global_load_dwordx4 v[6:9], v[14:15], off
	global_load_dwordx4 v[22:25], v[18:19], off offset:16 nt
	global_load_dwordx4 v[26:29], v[18:19], off nt
	global_load_dwordx4 v[10:13], v[14:15], off offset:528
	s_nop 0
	global_load_dwordx4 v[14:17], v[14:15], off offset:512
	s_nop 0
	global_load_dwordx4 v[30:33], v[18:19], off offset:528 nt
	global_load_dwordx4 v[182:185], v[18:19], off offset:512 nt
	global_load_dwordx4 v[186:189], v[204:205], off nt
	global_load_dwordx4 v[196:199], v[204:205], off offset:16 nt
	global_load_dwordx4 v[200:203], v[204:205], off offset:512 nt
	s_nop 0
	global_load_dwordx4 v[204:207], v[204:205], off offset:528 nt
	s_add_i32 s27, s25, 0xffff8000
	s_ashr_i32 s36, s25, 31
	s_cmpk_lt_i32 s34, 0x80
	s_cselect_b32 s37, s36, 0
	s_cselect_b32 s36, s25, s27
	s_cselect_b32 s25, s67, s65
	s_cselect_b32 s27, s66, s64
	s_lshl_b64 s[36:37], s[36:37], 11
	s_add_u32 s36, s27, s36
	s_addc_u32 s37, s25, s37
	v_or_b32_e32 v212, 32, v208
	v_lshl_add_u64 v[214:215], s[36:37], 0, v[172:173]
	v_ashrrev_i32_e32 v213, 31, v212
	v_lshl_add_u64 v[20:21], v[20:21], 1, v[214:215]
	v_lshlrev_b64 v[212:213], 12, v[212:213]
	v_add_co_u32_e32 v214, vcc, s58, v20
	v_lshl_add_u64 v[212:213], v[210:211], 0, v[212:213]
	s_nop 0
	v_addc_co_u32_e32 v215, vcc, 0, v21, vcc
	v_or_b32_e32 v248, 48, v208
	v_ashrrev_i32_e32 v249, 31, v248
	v_lshlrev_b64 v[248:249], 12, v[248:249]
	v_lshl_add_u64 v[250:251], v[210:211], 0, v[248:249]
	global_load_dwordx4 v[216:219], v[212:213], off nt
	global_load_dwordx4 v[220:223], v[212:213], off offset:16 nt
	global_load_dwordx4 v[224:227], v[212:213], off offset:528 nt
	global_load_dwordx4 v[228:231], v[212:213], off offset:512 nt
	global_load_dwordx4 v[232:235], v[250:251], off nt
	global_load_dwordx4 v[236:239], v[250:251], off offset:16 nt
	global_load_dwordx4 v[240:243], v[250:251], off offset:512 nt
	global_load_dwordx4 v[244:247], v[250:251], off offset:528 nt
	s_waitcnt vmcnt(8)
	v_pk_fma_f32 v[156:157], v[156:157], v[4:5], v[24:25]
	v_pk_fma_f32 v[28:29], v[160:161], v[8:9], v[28:29]
	v_pk_fma_f32 v[134:135], v[134:135], v[14:15], v[200:201]
	v_pk_fma_f32 v[26:27], v[158:159], v[6:7], v[26:27]
	v_pk_fma_f32 v[24:25], v[154:155], v[2:3], v[22:23]
	v_pk_fma_f32 v[32:33], v[140:141], v[12:13], v[32:33]
	v_pk_fma_f32 v[140:141], v[150:151], v[6:7], v[186:187]
	v_pk_fma_f32 v[150:151], v[132:133], v[12:13], v[206:207]
	v_pk_fma_f32 v[132:133], v[130:131], v[10:11], v[204:205]
	v_cvt_pk_bf16_f32 v130, v134, v135
	v_or_b32_e32 v134, 48, v208
	v_pk_fma_f32 v[144:145], v[144:145], v[16:17], v[184:185]
	v_pk_fma_f32 v[142:143], v[142:143], v[14:15], v[182:183]
	v_pk_fma_f32 v[30:31], v[138:139], v[10:11], v[30:31]
	v_pk_fma_f32 v[138:139], v[152:153], v[8:9], v[188:189]
	v_pk_fma_f32 v[148:149], v[148:149], v[4:5], v[198:199]
	v_pk_fma_f32 v[146:147], v[146:147], v[2:3], v[196:197]
	v_pk_fma_f32 v[136:137], v[136:137], v[16:17], v[202:203]
	v_cvt_pk_bf16_f32 v22, v26, v27
	v_cvt_pk_bf16_f32 v23, v28, v29
	v_cvt_pk_bf16_f32 v24, v24, v25
	v_cvt_pk_bf16_f32 v25, v156, v157
	v_ashrrev_i32_e32 v135, 31, v134
	v_cvt_pk_bf16_f32 v26, v142, v143
	v_cvt_pk_bf16_f32 v27, v144, v145
	v_cvt_pk_bf16_f32 v28, v30, v31
	v_cvt_pk_bf16_f32 v29, v32, v33
	v_cvt_pk_bf16_f32 v30, v140, v141
	v_cvt_pk_bf16_f32 v31, v138, v139
	v_cvt_pk_bf16_f32 v32, v146, v147
	v_cvt_pk_bf16_f32 v33, v148, v149
	v_cvt_pk_bf16_f32 v131, v136, v137
	v_cvt_pk_bf16_f32 v132, v132, v133
	v_cvt_pk_bf16_f32 v133, v150, v151
	global_store_dwordx4 v[20:21], v[22:25], off
	global_store_dwordx4 v[20:21], v[26:29], off offset:256
	global_store_dwordx4 v[214:215], v[30:33], off
	global_store_dwordx4 v[214:215], v[130:133], off offset:256
	v_add_co_u32_e32 v152, vcc, s70, v18
	v_lshl_add_u64 v[150:151], v[18:19], 0, s[6:7]
	s_nop 0
	v_addc_co_u32_e32 v153, vcc, 0, v19, vcc
	v_add_co_u32_e32 v154, vcc, s51, v20
	s_waitcnt vmcnt(4)
; __device__ __forceinline__ unsigned cvt_pk_bf16(float lo, float hi) { const f32x2_t v = {lo, hi}; return __builtin_bit_cast(unsigned, __builtin_convertvector(v, bf16x2_t)); }
;     __device__ __forceinline__ void operator()(const f32x4 (&acc)[2][2][4][2], const Unit& u, int wr, int wc, int fr, int fq) const {
;     ...
;         for (int ai = 0; ai < 2; ++ai)
; #pragma unroll
;             for (int mh = 0; mh < 2; ++mh) {
;                 f32x4 xv[2][2][2];
; #pragma unroll
;                 for (int m2 = 0; m2 < 2; ++m2) { const size_t off = (size_t)(row0 + ai * 128 + (2 * mh + m2) * 16) * D + col0;
; #pragma unroll
;                     for (int bj = 0; bj < 2; ++bj) { xv[m2][bj][0] = __builtin_nontemporal_load((const f32x4*)(x + off + bj * 128)); xv[m2][bj][1] = __builtin_nontemporal_load((const f32x4*)(x + off + bj * 128 + 4)); } }
; #pragma unroll
;                 for (int m2 = 0; m2 < 2; ++m2) { const int m = 2 * mh + m2;
; #pragma unroll
;                     for (int bj = 0; bj < 2; ++bj) {
;                         const f32x4 h0 = xv[m2][bj][0] + g[bj][0] * acc[ai][bj][m][0], h1 = xv[m2][bj][1] + g[bj][1] * acc[ai][bj][m][1];
;                         u32x4 w; w.x = cvt_pk_bf16(h0[0], h0[1]); w.y = cvt_pk_bf16(h0[2], h0[3]); w.z = cvt_pk_bf16(h1[0], h1[1]); w.w = cvt_pk_bf16(h1[2], h1[3]);
;                         *(u32x4*)(hb + (size_t)(ai * 128 + m * 16) * D + bj * 128) = w; } } }
	v_pk_fma_f32 v[218:219], v[128:129], v[8:9], v[218:219]
	v_addc_co_u32_e32 v155, vcc, 0, v21, vcc
	v_add_co_u32_e32 v156, vcc, s56, v20
	v_pk_fma_f32 v[216:217], v[126:127], v[6:7], v[216:217]
	s_nop 0
	v_addc_co_u32_e32 v157, vcc, 0, v21, vcc
	v_pk_fma_f32 v[222:223], v[124:125], v[4:5], v[222:223]
	v_pk_fma_f32 v[220:221], v[122:123], v[2:3], v[220:221]
	v_pk_fma_f32 v[102:103], v[102:103], v[14:15], v[240:241]
	v_pk_fma_f32 v[112:113], v[112:113], v[16:17], v[230:231]
	v_pk_fma_f32 v[110:111], v[110:111], v[14:15], v[228:229]
	v_pk_fma_f32 v[226:227], v[108:109], v[12:13], v[226:227]
	v_pk_fma_f32 v[224:225], v[106:107], v[10:11], v[224:225]
	v_pk_fma_f32 v[106:107], v[120:121], v[8:9], v[234:235]
	v_pk_fma_f32 v[108:109], v[118:119], v[6:7], v[232:233]
	v_pk_fma_f32 v[116:117], v[116:117], v[4:5], v[238:239]
	v_pk_fma_f32 v[114:115], v[114:115], v[2:3], v[236:237]
	v_pk_fma_f32 v[104:105], v[104:105], v[16:17], v[242:243]
	v_pk_fma_f32 v[118:119], v[100:101], v[12:13], v[246:247]
	v_pk_fma_f32 v[100:101], v[98:99], v[10:11], v[244:245]
	v_cvt_pk_bf16_f32 v216, v216, v217
	v_cvt_pk_bf16_f32 v217, v218, v219
	v_cvt_pk_bf16_f32 v218, v220, v221
	v_cvt_pk_bf16_f32 v219, v222, v223
	v_cvt_pk_bf16_f32 v98, v102, v103
	v_add_co_u32_e32 v102, vcc, s71, v18
	v_cvt_pk_bf16_f32 v220, v110, v111
	v_cvt_pk_bf16_f32 v221, v112, v113
	v_cvt_pk_bf16_f32 v222, v224, v225
	v_cvt_pk_bf16_f32 v223, v226, v227
	v_cvt_pk_bf16_f32 v224, v108, v109
	v_cvt_pk_bf16_f32 v225, v106, v107
	v_cvt_pk_bf16_f32 v226, v114, v115
	v_cvt_pk_bf16_f32 v227, v116, v117
	v_cvt_pk_bf16_f32 v99, v104, v105
	v_cvt_pk_bf16_f32 v100, v100, v101
	v_cvt_pk_bf16_f32 v101, v118, v119
	global_store_dwordx4 v[154:155], v[216:219], off
	global_store_dwordx4 v[154:155], v[220:223], off offset:256
	global_store_dwordx4 v[156:157], v[224:227], off
	global_store_dwordx4 v[156:157], v[98:101], off offset:256
	v_addc_co_u32_e32 v103, vcc, 0, v19, vcc
	global_load_dwordx4 v[22:25], v[152:153], off nt
	global_load_dwordx4 v[26:29], v[150:151], off offset:528 nt
	global_load_dwordx4 v[30:33], v[150:151], off offset:16 nt
	global_load_dwordx4 v[98:101], v[150:151], off offset:512 nt
	v_lshl_add_u64 v[114:115], v[18:19], 0, s[18:19]
	global_load_dwordx4 v[102:105], v[102:103], off nt
	s_nop 0
	global_load_dwordx4 v[106:109], v[114:115], off offset:16 nt
	global_load_dwordx4 v[110:113], v[114:115], off offset:512 nt
	s_nop 0
	global_load_dwordx4 v[114:117], v[114:115], off offset:528 nt
	v_add_co_u32_e32 v120, vcc, s74, v18
	v_lshl_add_u64 v[118:119], v[18:19], 0, s[20:21]
	s_nop 0
	v_addc_co_u32_e32 v121, vcc, 0, v19, vcc
	v_add_co_u32_e32 v122, vcc, s72, v20
	s_waitcnt vmcnt(7)
	v_pk_fma_f32 v[24:25], v[80:81], v[8:9], v[24:25]
	v_addc_co_u32_e32 v123, vcc, 0, v21, vcc
	v_add_co_u32_e32 v124, vcc, s73, v20
	v_pk_fma_f32 v[22:23], v[78:79], v[6:7], v[22:23]
	s_nop 0
	v_addc_co_u32_e32 v125, vcc, 0, v21, vcc
	s_waitcnt vmcnt(5)
	v_pk_fma_f32 v[32:33], v[76:77], v[4:5], v[32:33]
	v_pk_fma_f32 v[30:31], v[74:75], v[2:3], v[30:31]
	s_waitcnt vmcnt(3)
	v_pk_fma_f32 v[70:71], v[70:71], v[6:7], v[102:103]
	v_pk_fma_f32 v[74:75], v[88:89], v[16:17], v[100:101]
	v_pk_fma_f32 v[76:77], v[86:87], v[14:15], v[98:99]
	v_pk_fma_f32 v[78:79], v[96:97], v[12:13], v[28:29]
	v_pk_fma_f32 v[28:29], v[94:95], v[10:11], v[26:27]
	v_pk_fma_f32 v[72:73], v[72:73], v[8:9], v[104:105]
	s_waitcnt vmcnt(2)
	v_pk_fma_f32 v[68:69], v[68:69], v[4:5], v[108:109]
	v_pk_fma_f32 v[66:67], v[66:67], v[2:3], v[106:107]
	s_waitcnt vmcnt(1)
	v_pk_fma_f32 v[80:81], v[84:85], v[16:17], v[112:113]
	v_pk_fma_f32 v[82:83], v[82:83], v[14:15], v[110:111]
	s_waitcnt vmcnt(0)
	v_pk_fma_f32 v[84:85], v[92:93], v[12:13], v[116:117]
	v_pk_fma_f32 v[86:87], v[90:91], v[10:11], v[114:115]
	v_cvt_pk_bf16_f32 v22, v22, v23
	v_cvt_pk_bf16_f32 v23, v24, v25
	v_cvt_pk_bf16_f32 v24, v30, v31
	v_cvt_pk_bf16_f32 v25, v32, v33
	v_cvt_pk_bf16_f32 v30, v70, v71
	v_add_co_u32_e32 v70, vcc, s75, v18
	v_cvt_pk_bf16_f32 v26, v76, v77
	v_cvt_pk_bf16_f32 v27, v74, v75
	v_cvt_pk_bf16_f32 v28, v28, v29
	v_cvt_pk_bf16_f32 v29, v78, v79
	v_cvt_pk_bf16_f32 v31, v72, v73
	v_cvt_pk_bf16_f32 v32, v66, v67
	v_cvt_pk_bf16_f32 v33, v68, v69
	v_cvt_pk_bf16_f32 v66, v82, v83
	v_cvt_pk_bf16_f32 v67, v80, v81
	v_cvt_pk_bf16_f32 v68, v86, v87
	v_cvt_pk_bf16_f32 v69, v84, v85
	global_store_dwordx4 v[122:123], v[22:25], off
	global_store_dwordx4 v[122:123], v[26:29], off offset:256
	global_store_dwordx4 v[124:125], v[30:33], off
	global_store_dwordx4 v[124:125], v[66:69], off offset:256
	v_addc_co_u32_e32 v71, vcc, 0, v19, vcc
	v_lshl_add_u64 v[18:19], v[18:19], 0, s[22:23]
	global_load_dwordx4 v[22:25], v[120:121], off nt
	global_load_dwordx4 v[26:29], v[118:119], off offset:528 nt
	global_load_dwordx4 v[30:33], v[118:119], off offset:16 nt
	global_load_dwordx4 v[66:69], v[118:119], off offset:512 nt
	s_andn2_b64 vcc, exec, s[4:5]
	global_load_dwordx4 v[70:73], v[70:71], off nt
	s_nop 0
	global_load_dwordx4 v[74:77], v[18:19], off offset:16 nt
	global_load_dwordx4 v[78:81], v[18:19], off offset:512 nt
	global_load_dwordx4 v[82:85], v[18:19], off offset:528 nt
	v_add_co_u32_e64 v18, s[4:5], s76, v20
	s_waitcnt vmcnt(7)
	v_pk_fma_f32 v[24:25], v[48:49], v[8:9], v[24:25]
	v_addc_co_u32_e64 v19, s[4:5], 0, v21, s[4:5]
	v_add_co_u32_e64 v20, s[4:5], s77, v20
	v_pk_fma_f32 v[22:23], v[46:47], v[6:7], v[22:23]
	s_nop 0
	v_addc_co_u32_e64 v21, s[4:5], 0, v21, s[4:5]
	s_waitcnt vmcnt(5)
	v_pk_fma_f32 v[32:33], v[44:45], v[4:5], v[32:33]
	v_pk_fma_f32 v[30:31], v[42:43], v[2:3], v[30:31]
	s_waitcnt vmcnt(4)
	v_pk_fma_f32 v[42:43], v[56:57], v[16:17], v[68:69]
	v_pk_fma_f32 v[44:45], v[54:55], v[14:15], v[66:67]
	v_pk_fma_f32 v[28:29], v[64:65], v[12:13], v[28:29]
	v_pk_fma_f32 v[26:27], v[62:63], v[10:11], v[26:27]
	s_waitcnt vmcnt(3)
	v_pk_fma_f32 v[40:41], v[40:41], v[8:9], v[72:73]
	v_pk_fma_f32 v[38:39], v[38:39], v[6:7], v[70:71]
	s_waitcnt vmcnt(2)
	v_pk_fma_f32 v[36:37], v[36:37], v[4:5], v[76:77]
	v_pk_fma_f32 v[34:35], v[34:35], v[2:3], v[74:75]
	s_waitcnt vmcnt(1)
	v_pk_fma_f32 v[16:17], v[52:53], v[16:17], v[80:81]
	v_pk_fma_f32 v[14:15], v[50:51], v[14:15], v[78:79]
	s_waitcnt vmcnt(0)
	v_pk_fma_f32 v[46:47], v[60:61], v[12:13], v[84:85]
	v_pk_fma_f32 v[48:49], v[58:59], v[10:11], v[82:83]
	v_cvt_pk_bf16_f32 v2, v22, v23
	v_cvt_pk_bf16_f32 v3, v24, v25
	v_cvt_pk_bf16_f32 v4, v30, v31
	v_cvt_pk_bf16_f32 v5, v32, v33
	s_mov_b64 s[4:5], -1
	v_cvt_pk_bf16_f32 v6, v44, v45
	v_cvt_pk_bf16_f32 v7, v42, v43
	v_cvt_pk_bf16_f32 v8, v26, v27
	v_cvt_pk_bf16_f32 v9, v28, v29
	v_cvt_pk_bf16_f32 v10, v38, v39
	v_cvt_pk_bf16_f32 v11, v40, v41
	v_cvt_pk_bf16_f32 v12, v34, v35
	v_cvt_pk_bf16_f32 v13, v36, v37
	v_cvt_pk_bf16_f32 v14, v14, v15
	v_cvt_pk_bf16_f32 v15, v16, v17
	v_cvt_pk_bf16_f32 v16, v48, v49
	v_cvt_pk_bf16_f32 v17, v46, v47
	global_store_dwordx4 v[18:19], v[2:5], off
	global_store_dwordx4 v[18:19], v[6:9], off offset:256
	global_store_dwordx4 v[20:21], v[10:13], off
	global_store_dwordx4 v[20:21], v[14:17], off offset:256
	s_cbranch_vccnz .LBB0_425
; #define PG8_BAR __builtin_amdgcn_s_barrier()
;     ...
;         cur = nxt; cA = nA; cB = nB; ++ui;
;         if constexpr (GATHER) { va[0][0] = vn[0][0]; va[0][1] = vn[0][1]; va[1][0] = vn[1][0]; va[1][1] = vn[1][1]; }
;         if constexpr (ALIGN_EPI) { if (wr == 1) PG8_BAR; }
	s_andn2_b64 vcc, exec, s[12:13]
	s_cbranch_vccnz .LBB0_424
	s_barrier
	s_branch .LBB0_424
